# final candidate code shifted by 8 bytes (two s_nop at entry): code-placement variant, function unchanged
# baseline (speedup 1.0000x reference)
_Z10fwd_kernel6Params:
	s_load_dword s11, s[0:1], 0xc8
	s_nop 0
	s_nop 0
	s_add_u32 s4, s0, 0xc8
	s_addc_u32 s5, s1, 0
	v_readfirstlane_b32 s10, v0
	v_writelane_b32 v255, s4, 0
	s_waitcnt lgkmcnt(0)
	s_and_b32 s3, s11, 7
	s_cmp_lg_u32 s3, 0
	v_writelane_b32 v255, s5, 1
	s_mov_b32 s3, s2
	s_cbranch_scc1 .LBB0_2
	s_ashr_i32 s4, s2, 31
	s_lshr_b32 s4, s4, 29
	s_add_i32 s4, s2, s4
	s_ashr_i32 s5, s4, 3
	s_and_b32 s4, s4, -8
	s_ashr_i32 s3, s11, 3
	s_sub_i32 s4, s2, s4
	s_mul_i32 s3, s3, s4
	s_add_i32 s3, s3, s5
